# baseline (speedup 1.0000x reference)
.Lkf_poll:
	global_load_dwordx4 v[42:45], v38, s[14:15] sc1
	global_load_dwordx2 v[48:49], v38, s[14:15] offset:16 sc1
	s_add_i32 s22, s22, -1
	s_waitcnt vmcnt(0)
	v_and_b32_e32 v36, 0xff, v42
	v_and_b32_e32 v37, 0xff, v44
	v_and_b32_e32 v41, 0xff, v48
	v_add3_u32 v36, v36, v37, v41
	v_cmp_ne_u32_e32 vcc, 24, v36
	s_cmp_eq_u32 s22, 0
	s_cbranch_scc1 .Lkf_poll_end
	s_cbranch_vccz .Lkf_poll_end
	s_branch .Lkf_poll
